# v56 + P0 weight copies: generic (non-fast) items issue the 8 element loads of a trip together (4 round trips per item instead of 32/64)
# speedup vs baseline: 1.0142x; 1.0015x over previous
.LBB6_135:
	s_add_u32 s8, s8, 0x109000
	s_addc_u32 s9, s9, 0
	s_cmp_lg_u32 s8, 0x424000
	v_add_u32_e32 v171, 0x840, v171
	s_cbranch_scc0 .LBB6_152
.LBB6_136:
	v_mov_b32_e32 v196, 0
	v_mov_b32_e32 v197, 0
	v_mov_b32_e32 v198, 0
	v_mov_b32_e32 v199, 0
	v_mov_b32_e32 v200, 0
	v_mov_b32_e32 v201, 0
	v_mov_b32_e32 v202, 0
	v_mov_b32_e32 v203, 0
	s_and_saveexec_b64 s[18:19], vcc
	s_cbranch_execz .Lp0s_std_skip
	v_lshl_add_u64 v[2:3], v[126:127], 0, s[8:9]
	global_load_dword v196, v[2:3], off
	v_lshl_add_u64 v[4:5], v[124:125], 0, s[8:9]
	global_load_dword v197, v[4:5], off
	v_lshl_add_u64 v[2:3], v[122:123], 0, s[8:9]
	global_load_dword v198, v[2:3], off
	v_lshl_add_u64 v[4:5], v[120:121], 0, s[8:9]
	global_load_dword v199, v[4:5], off
	v_lshl_add_u64 v[2:3], v[118:119], 0, s[8:9]
	global_load_dword v200, v[2:3], off
	v_lshl_add_u64 v[4:5], v[116:117], 0, s[8:9]
	global_load_dword v201, v[4:5], off
	v_lshl_add_u64 v[2:3], v[114:115], 0, s[8:9]
	global_load_dword v202, v[2:3], off
	v_lshl_add_u64 v[4:5], v[112:113], 0, s[8:9]
	global_load_dword v203, v[4:5], off
.Lp0s_std_skip:
	s_or_b64 exec, exec, s[18:19]
	s_waitcnt vmcnt(0)
	ds_write_b32 v171, v196
	ds_write_b32 v171, v197 offset:264
	ds_write_b32 v171, v198 offset:528
	ds_write_b32 v171, v199 offset:792
	ds_write_b32 v171, v200 offset:1056
	ds_write_b32 v171, v201 offset:1320
	ds_write_b32 v171, v202 offset:1584
	ds_write_b32 v171, v203 offset:1848
	s_branch .LBB6_135

.LBB6_244:
	s_add_u32 s24, s24, 0xc000
	s_addc_u32 s25, s25, 0
	s_add_u32 s26, s26, 64
	s_addc_u32 s27, s27, 0
	s_cmp_lg_u32 s24, 0x30000
	v_add_u32_e32 v88, 0x840, v88
	s_cbranch_scc0 .LBB6_277
.LBB6_245:
	v_mov_b32_e32 v196, 0
	v_mov_b32_e32 v197, 0
	v_mov_b32_e32 v198, 0
	v_mov_b32_e32 v199, 0
	v_mov_b32_e32 v200, 0
	v_mov_b32_e32 v201, 0
	v_mov_b32_e32 v202, 0
	v_mov_b32_e32 v203, 0
	v_mov_b32_e32 v204, 1.0
	v_mov_b32_e32 v205, 1.0
	v_mov_b32_e32 v206, 1.0
	v_mov_b32_e32 v207, 1.0
	v_mov_b32_e32 v208, 1.0
	v_mov_b32_e32 v209, 1.0
	v_mov_b32_e32 v210, 1.0
	v_mov_b32_e32 v211, 1.0
	s_and_saveexec_b64 s[6:7], s[4:5]
	s_cbranch_execz .Lp0s_uq_skipw
	v_lshl_add_u64 v[86:87], v[82:83], 0, s[24:25]
	global_load_dword v196, v[86:87], off
	v_lshl_add_u64 v[90:91], v[80:81], 0, s[24:25]
	global_load_dword v197, v[90:91], off
	v_lshl_add_u64 v[86:87], v[78:79], 0, s[24:25]
	global_load_dword v198, v[86:87], off
	v_lshl_add_u64 v[90:91], v[76:77], 0, s[24:25]
	global_load_dword v199, v[90:91], off
	v_lshl_add_u64 v[86:87], v[74:75], 0, s[24:25]
	global_load_dword v200, v[86:87], off
	v_lshl_add_u64 v[90:91], v[72:73], 0, s[24:25]
	global_load_dword v201, v[90:91], off
	v_lshl_add_u64 v[86:87], v[70:71], 0, s[24:25]
	global_load_dword v202, v[86:87], off
	v_lshl_add_u64 v[90:91], v[66:67], 0, s[24:25]
	global_load_dword v203, v[90:91], off
.Lp0s_uq_skipw:
	s_or_b64 exec, exec, s[6:7]
	s_andn2_b64 vcc, exec, s[16:17]
	s_cbranch_vccnz .Lp0s_uq_skipk
	v_lshl_add_u64 v[90:91], s[26:27], 0, v[84:85]
	global_load_dword v204, v[90:91], off
	v_lshl_add_u64 v[86:87], s[26:27], 0, v[68:69]
	global_load_dword v205, v[86:87], off offset:8
	global_load_dword v206, v[86:87], off offset:16
	global_load_dword v207, v[86:87], off offset:24
	global_load_dword v208, v[86:87], off offset:32
	global_load_dword v209, v[86:87], off offset:40
	global_load_dword v210, v[86:87], off offset:48
	global_load_dword v211, v[86:87], off offset:56
.Lp0s_uq_skipk:
	s_waitcnt vmcnt(0)
	v_mul_f32_e32 v196, v196, v204
	v_mul_f32_e32 v197, v197, v205
	v_mul_f32_e32 v198, v198, v206
	v_mul_f32_e32 v199, v199, v207
	v_mul_f32_e32 v200, v200, v208
	v_mul_f32_e32 v201, v201, v209
	v_mul_f32_e32 v202, v202, v210
	v_mul_f32_e32 v203, v203, v211
	ds_write_b32 v88, v196
	ds_write_b32 v88, v197 offset:264
	ds_write_b32 v88, v198 offset:528
	ds_write_b32 v88, v199 offset:792
	ds_write_b32 v88, v200 offset:1056
	ds_write_b32 v88, v201 offset:1320
	ds_write_b32 v88, v202 offset:1584
	ds_write_b32 v88, v203 offset:1848
	s_branch .LBB6_244
